# recheck: code-index constant setup moved behind the flagged-row loads
# baseline (speedup 1.0000x reference)
.LBB0_107:
	s_waitcnt vmcnt(1)
	v_lshrrev_b32_e32 v177, 4, v0
	v_and_b32_e32 v166, 63, v0
	s_setprio 0
	s_waitcnt vmcnt(0)
	v_mov_b32_e32 v66, 0x21d44
	ds_read_b32 v183, v66
	s_mov_b32 s25, 0
	v_mbcnt_lo_u32_b32 v176, -1, 0
	s_waitcnt lgkmcnt(0)
	v_cmp_eq_u32_e32 vcc, 0, v183
	s_cbranch_vccnz .LBB0_455
	v_mov_b32_e32 v169, 0
	v_mov_b32_e32 v179, v169
	v_lshlrev_b32_e32 v67, 2, v184
	v_lshlrev_b32_e32 v68, 10, v181
	v_lshl_add_u64 v[170:171], s[20:21], 0, v[178:179]
	v_mov_b32_e32 v66, 0x21c00
	v_lshl_add_u64 v[172:173], s[12:13], 0, v[178:179]
	v_or3_b32 v179, s3, v67, v68
	v_mov_b32_e32 v246, 0x1c400
	v_mov_b32_e32 v174, -1
	v_cmp_gt_u32_e64 s[4:5], 32, v0
	v_lshl_add_u32 v185, v0, 3, v66
	v_cmp_eq_u32_e64 s[6:7], 0, v1
	v_lshl_or_b32 v184, v177, 3, v66
	v_lshl_or_b32 v247, v177, 2, v246
	v_mov_b32_e32 v248, 0x21d40
	s_movk_i32 s3, 0x90
	s_movk_i32 s20, 0x800
	s_movk_i32 s21, 0x3ff0
	s_movk_i32 s26, 0xfc00
	v_mov_b32_e32 v249, 0x21400
	v_mov_b32_e32 v175, v174
	v_mov_b32_e32 v250, 0x20400
	v_mbcnt_hi_u32_b32 v251, -1, v176
	v_mov_b32_e32 v252, 0x20c00
	s_branch .LBB0_110

.LBB0_116:
	s_or_b64 exec, exec, s[0:1]
	v_or_b32_e32 v66, s25, v181
	v_cmp_lt_u32_e32 vcc, v66, v183
	v_mov_b32_e32 v67, 0
	v_or_b32_e32 v186, 8, v179
	v_or_b32_e32 v187, 9, v179
	v_or_b32_e32 v188, 10, v179
	v_or_b32_e32 v189, 11, v179
	v_or_b32_e32 v190, 16, v179
	v_or_b32_e32 v191, 17, v179
	v_or_b32_e32 v192, 18, v179
	v_or_b32_e32 v193, 19, v179
	v_or_b32_e32 v194, 24, v179
	v_or_b32_e32 v195, 25, v179
	v_or_b32_e32 v196, 26, v179
	v_or_b32_e32 v197, 27, v179
	v_or_b32_e32 v198, 32, v179
	v_or_b32_e32 v199, 33, v179
	v_or_b32_e32 v200, 34, v179
	v_or_b32_e32 v201, 35, v179
	v_or_b32_e32 v202, 40, v179
	v_or_b32_e32 v203, 41, v179
	v_or_b32_e32 v204, 42, v179
	v_or_b32_e32 v205, 43, v179
	v_or_b32_e32 v206, 48, v179
	v_or_b32_e32 v207, 49, v179
	v_or_b32_e32 v208, 50, v179
	v_or_b32_e32 v209, 51, v179
	v_or_b32_e32 v210, 56, v179
	v_or_b32_e32 v211, 57, v179
	v_or_b32_e32 v212, 58, v179
	v_or_b32_e32 v213, 59, v179
	v_or_b32_e32 v214, 64, v179
	v_or_b32_e32 v215, 0x41, v179
	v_or_b32_e32 v216, 0x42, v179
	v_or_b32_e32 v217, 0x43, v179
	v_or_b32_e32 v218, 0x48, v179
	v_or_b32_e32 v219, 0x49, v179
	v_or_b32_e32 v220, 0x4a, v179
	v_or_b32_e32 v221, 0x4b, v179
	v_or_b32_e32 v222, 0x50, v179
	v_or_b32_e32 v223, 0x51, v179
	v_or_b32_e32 v224, 0x52, v179
	v_or_b32_e32 v225, 0x53, v179
	v_or_b32_e32 v226, 0x58, v179
	v_or_b32_e32 v227, 0x59, v179
	v_or_b32_e32 v228, 0x5a, v179
	v_or_b32_e32 v229, 0x5b, v179
	v_or_b32_e32 v230, 0x60, v179
	v_or_b32_e32 v231, 0x61, v179
	v_or_b32_e32 v232, 0x62, v179
	v_or_b32_e32 v233, 0x63, v179
	v_or_b32_e32 v234, 0x68, v179
	v_or_b32_e32 v235, 0x69, v179
	v_or_b32_e32 v236, 0x6a, v179
	v_or_b32_e32 v237, 0x6b, v179
	v_or_b32_e32 v238, 0x70, v179
	v_or_b32_e32 v239, 0x71, v179
	v_or_b32_e32 v240, 0x72, v179
	v_or_b32_e32 v241, 0x73, v179
	v_or_b32_e32 v242, 0x78, v179
	v_or_b32_e32 v243, 0x79, v179
	v_or_b32_e32 v244, 0x7a, v179
	v_or_b32_e32 v245, 0x7b, v179
	s_waitcnt lgkmcnt(0)
	s_barrier
	s_and_saveexec_b64 s[0:1], vcc
	s_cbranch_execz .LBB0_118
	v_lshl_add_u32 v67, v66, 2, v249
	ds_read_b32 v67, v67
	s_waitcnt lgkmcnt(0)
	v_mul_lo_u32 v67, v67, s3
